# P3 qknorm rows re-dealt: CUs 0-127 (S5 state GEMM CUs) skip qknorm, CUs 128-255 take four 4-row steps per wave
# baseline (speedup 1.0000x reference)
; __device__ __forceinline__ void qknorm_body(const Args& a, int wave, int lane, int G, int bid) {
;     const int gw = bid * NWAVES + wave, NGW = G * NWAVES;
;     {   bf16* Q = (bf16*)(a.ws + WS_Q); bf16* K = (bf16*)(a.ws + WS_K); const float* qg = a.in[I_QG]; const float* kg = a.in[I_KG];
;         const float qs = 0.08838834764831845f * 1.4426950408889634f;
;         const int l32 = lane & 31; float qgv[16], kgv[8];
; #pragma unroll
;         for (int e = 0; e < 16; ++e) qgv[e] = qg[((16 * lane) & 127) + e];
; #pragma unroll
;         for (int e = 0; e < 8; ++e) kgv[e] = kg[((8 * l32) & 127) + e];
;         for (int row0 = gw; row0 < T; row0 += 4 * NGW) {
.LBB0_608:
	s_lshl_b32 s0, s84, 3
	v_readlane_b32 s1, v251, 12
	s_add_i32 s2, s1, s0
	s_cmpk_gt_i32 s2, 0x3fff
	v_lshlrev_b32_e32 v79, 3, v178
	s_cbranch_scc1 .LBB0_625
	s_cmpk_lg_i32 s88, 0x100
	s_cbranch_scc1 .Lqk_go
	s_cmpk_lt_i32 s84, 0x80
	s_cbranch_scc1 .LBB0_625
.Lqk_go:
	v_readlane_b32 s36, v250, 17
	v_lshlrev_b32_e32 v2, 6, v178
	v_readlane_b32 s48, v250, 29
	v_readlane_b32 s49, v250, 30
	s_waitcnt vmcnt(0)
	v_and_b32_e32 v26, 0x1c0, v2
	v_and_b32_e32 v2, 0x78, v79
	v_readlane_b32 s50, v250, 31
	v_readlane_b32 s51, v250, 32
	s_mov_b64 s[12:13], s[48:49]
	v_lshlrev_b32_e32 v27, 2, v2
	s_mov_b64 s[14:15], s[50:51]
	global_load_dwordx4 v[2:5], v26, s[12:13] offset:48
	global_load_dwordx4 v[6:9], v26, s[12:13] offset:32
	global_load_dwordx4 v[10:13], v26, s[12:13] offset:16
	global_load_dwordx4 v[14:17], v26, s[12:13]
	global_load_dwordx4 v[18:21], v27, s[14:15] offset:16
	global_load_dwordx4 v[22:25], v27, s[14:15]
	v_lshlrev_b32_e32 v26, 5, v178
	v_mov_b32_e32 v27, 0
	v_lshl_add_u64 v[28:29], s[82:83], 0, v[26:27]
	v_and_b32_e32 v26, 0xf8, v79
	s_mov_b64 s[0:1], 0x13100000
	v_lshlrev_b32_e32 v26, 1, v26
	v_lshl_add_u64 v[62:63], v[28:29], 0, s[0:1]
	v_lshl_add_u64 v[26:27], s[82:83], 0, v[26:27]
	s_mov_b64 s[0:1], 0x15100000
	v_lshl_add_u64 v[64:65], v[26:27], 0, s[0:1]
	v_mbcnt_lo_u32_b32 v26, -1, 0
	v_mbcnt_hi_u32_b32 v26, -1, v26
	v_and_b32_e32 v28, 64, v26
	v_xor_b32_e32 v27, 1, v26
	v_add_u32_e32 v28, 64, v28
	v_cmp_lt_i32_e32 vcc, v27, v28
	s_lshl_b32 s14, s88, 3
	v_cmp_gt_u32_e64 s[0:1], 32, v178
	v_cndmask_b32_e32 v27, v26, v27, vcc
	v_lshlrev_b32_e32 v80, 2, v27
	v_xor_b32_e32 v27, 2, v26
	v_cmp_lt_i32_e32 vcc, v27, v28
	s_lshl_b32 s15, s88, 4
	s_mul_i32 s16, s88, 24
	v_cndmask_b32_e32 v27, v26, v27, vcc
	v_lshlrev_b32_e32 v81, 2, v27
	v_xor_b32_e32 v27, 4, v26
	v_cmp_lt_i32_e32 vcc, v27, v28
	v_mov_b32_e32 v84, 0x358637bd
	s_mov_b32 s17, 0xf800000
	v_cndmask_b32_e32 v27, v26, v27, vcc
	v_lshlrev_b32_e32 v82, 2, v27
	v_xor_b32_e32 v27, 8, v26
	v_cmp_lt_i32_e32 vcc, v27, v28
	v_mov_b32_e32 v85, 0x260
	s_mov_b32 s18, 0x3e0293ee
	v_cndmask_b32_e32 v26, v26, v27, vcc
	v_lshlrev_b32_e32 v83, 2, v26
	v_readlane_b32 s37, v250, 18
	v_readlane_b32 s38, v250, 19
	v_readlane_b32 s39, v250, 20
	v_readlane_b32 s40, v250, 21
	v_readlane_b32 s41, v250, 22
	v_readlane_b32 s42, v250, 23
	v_readlane_b32 s43, v250, 24
	v_readlane_b32 s44, v250, 25
	v_readlane_b32 s45, v250, 26
	v_readlane_b32 s46, v250, 27
	v_readlane_b32 s47, v250, 28
	s_branch .LBB0_612

; __device__ __forceinline__ void qknorm_body(const Args& a, int wave, int lane, int G, int bid) {
;     ...
;         for (int row0 = gw; row0 < T; row0 += 4 * NGW) {
;             v4u qa[4], qb[4], ka[4];
; #pragma unroll
;             for (int u = 0; u < 4; ++u) { const int row = min(row0 + u * NGW, T - 1); const v4u* qp = (const v4u*)(Q + (size_t)row * 1024 + 16 * lane); qa[u] = qp[0]; qb[u] = qp[1]; ka[u] = *(const v4u*)(K + (size_t)row * 256 + 8 * l32); }
; #pragma unroll
;             for (int u = 0; u < 4; ++u) { const int row = row0 + u * NGW; if (row < T) {
.LBB0_611:
	s_add_i32 s3, s4, s14
	s_add_i32 s3, s3, s14
	s_add_i32 s3, s3, s14
	s_mov_b32 s2, s3
	s_cmpk_lt_i32 s2, 0x4000
	s_cbranch_scc1 .LBB0_612
	s_cmpk_lg_i32 s88, 0x100
	s_cbranch_scc1 .LBB0_625
	s_sub_i32 s2, s4, s14
	s_bitcmp0_b32 s2, 10
	s_cbranch_scc1 .LBB0_625
	s_addk_i32 s2, 0xdc00
	s_branch .LBB0_612
